# baseline (speedup 1.0000x reference)
.LBB3_21:
	v_add_co_u32_e32 v212, vcc, s15, v180
	s_waitcnt vmcnt(15) lgkmcnt(3)
	v_mfma_f32_32x32x16_f16 v[50:65], v[118:121], v[174:177], v[50:65]
	v_addc_co_u32_e32 v213, vcc, 0, v181, vcc
	v_lshl_add_u64 v[214:215], v[180:181], 0, s[8:9]
	s_waitcnt lgkmcnt(2)
	v_mfma_f32_32x32x16_f16 v[34:49], v[118:121], v[170:173], v[34:49]
	global_load_dwordx4 v[118:121], v[180:181], off
	s_waitcnt vmcnt(15)
	v_mfma_f32_32x32x16_f16 v[18:33], v[98:101], v[174:177], v[18:33]
	v_mfma_f32_32x32x16_f16 v[2:17], v[98:101], v[170:173], v[2:17]
	global_load_dwordx4 v[98:101], v[212:213], off offset:-4096
	ds_read_b128 v[170:173], v210
	ds_read_b128 v[174:177], v210 offset:33280
	s_waitcnt vmcnt(15) lgkmcnt(3)
	v_mfma_f32_32x32x16_f16 v[50:65], v[114:117], v[166:169], v[50:65]
	s_waitcnt lgkmcnt(2)
	v_mfma_f32_32x32x16_f16 v[34:49], v[114:117], v[162:165], v[34:49]
	global_load_dwordx4 v[114:117], v[180:181], off offset:1024
	s_waitcnt vmcnt(15)
	v_mfma_f32_32x32x16_f16 v[18:33], v[102:105], v[166:169], v[18:33]
	v_mfma_f32_32x32x16_f16 v[2:17], v[102:105], v[162:165], v[2:17]
	global_load_dwordx4 v[102:105], v[214:215], off offset:1024
	ds_read_b128 v[162:165], v210 offset:32
	ds_read_b128 v[166:169], v210 offset:33312
	s_waitcnt vmcnt(15) lgkmcnt(3)
	v_mfma_f32_32x32x16_f16 v[50:65], v[122:125], v[170:173], v[50:65]
	s_waitcnt lgkmcnt(2)
	v_mfma_f32_32x32x16_f16 v[34:49], v[122:125], v[174:177], v[34:49]
	global_load_dwordx4 v[122:125], v[180:181], off offset:2048
	s_waitcnt vmcnt(15)
	v_mfma_f32_32x32x16_f16 v[18:33], v[106:109], v[170:173], v[18:33]
	v_mfma_f32_32x32x16_f16 v[2:17], v[106:109], v[174:177], v[2:17]
	global_load_dwordx4 v[106:109], v[214:215], off offset:2048
	ds_read_b128 v[170:173], v210 offset:64
	ds_read_b128 v[174:177], v210 offset:33344
	s_waitcnt vmcnt(15) lgkmcnt(3)
	v_mfma_f32_32x32x16_f16 v[50:65], v[126:129], v[162:165], v[50:65]
	s_waitcnt lgkmcnt(2)
	v_mfma_f32_32x32x16_f16 v[34:49], v[126:129], v[166:169], v[34:49]
	global_load_dwordx4 v[126:129], v[180:181], off offset:3072
	s_waitcnt vmcnt(15)
	v_mfma_f32_32x32x16_f16 v[18:33], v[110:113], v[162:165], v[18:33]
	v_mfma_f32_32x32x16_f16 v[2:17], v[110:113], v[166:169], v[2:17]
	global_load_dwordx4 v[110:113], v[214:215], off offset:3072
	ds_read_b128 v[162:165], v210 offset:96
	ds_read_b128 v[166:169], v210 offset:33376
	s_waitcnt vmcnt(15) lgkmcnt(3)
	v_mfma_f32_32x32x16_f16 v[50:65], v[146:149], v[170:173], v[50:65]
	v_lshl_add_u64 v[214:215], v[180:181], 0, s[12:13]
	s_waitcnt lgkmcnt(2)
	v_mfma_f32_32x32x16_f16 v[34:49], v[146:149], v[174:177], v[34:49]
	v_add_co_u32_e32 v146, vcc, s3, v180
	s_nop 1
	v_addc_co_u32_e32 v147, vcc, 0, v181, vcc
	s_waitcnt vmcnt(14)
	v_mfma_f32_32x32x16_f16 v[18:33], v[134:137], v[170:173], v[18:33]
	v_mfma_f32_32x32x16_f16 v[2:17], v[134:137], v[174:177], v[2:17]
	global_load_dwordx4 v[146:149], v[146:147], off
	s_nop 0
	global_load_dwordx4 v[134:137], v[212:213], off
	ds_read_b128 v[170:173], v210 offset:128
	ds_read_b128 v[174:177], v210 offset:33408
	v_lshl_add_u64 v[212:213], v[180:181], 0, s[10:11]
	s_waitcnt vmcnt(15) lgkmcnt(3)
	v_mfma_f32_32x32x16_f16 v[50:65], v[142:145], v[162:165], v[50:65]
	s_waitcnt lgkmcnt(2)
	v_mfma_f32_32x32x16_f16 v[34:49], v[142:145], v[166:169], v[34:49]
	s_waitcnt vmcnt(14)
	v_mfma_f32_32x32x16_f16 v[18:33], v[130:133], v[162:165], v[18:33]
	v_mfma_f32_32x32x16_f16 v[2:17], v[130:133], v[166:169], v[2:17]
	global_load_dwordx4 v[142:145], v[212:213], off offset:1024
	global_load_dwordx4 v[130:133], v[214:215], off offset:1024
	ds_read_b128 v[162:165], v210 offset:160
	ds_read_b128 v[166:169], v210 offset:33440
	s_waitcnt vmcnt(15) lgkmcnt(3)
	v_mfma_f32_32x32x16_f16 v[50:65], v[150:153], v[170:173], v[50:65]
	s_waitcnt lgkmcnt(2)
	v_mfma_f32_32x32x16_f16 v[34:49], v[150:153], v[174:177], v[34:49]
	s_waitcnt vmcnt(14)
	v_mfma_f32_32x32x16_f16 v[18:33], v[138:141], v[170:173], v[18:33]
	v_mfma_f32_32x32x16_f16 v[2:17], v[138:141], v[174:177], v[2:17]
	global_load_dwordx4 v[150:153], v[212:213], off offset:2048
	global_load_dwordx4 v[138:141], v[214:215], off offset:2048
	ds_read_b128 v[174:177], v210 offset:192
	ds_read_b128 v[170:173], v210 offset:33472
	s_waitcnt vmcnt(15) lgkmcnt(3)
	v_mfma_f32_32x32x16_f16 v[50:65], v[158:161], v[162:165], v[50:65]
	s_waitcnt lgkmcnt(2)
	v_mfma_f32_32x32x16_f16 v[34:49], v[158:161], v[166:169], v[34:49]
	s_waitcnt vmcnt(14)
	v_mfma_f32_32x32x16_f16 v[18:33], v[154:157], v[162:165], v[18:33]
	v_mfma_f32_32x32x16_f16 v[2:17], v[154:157], v[166:169], v[2:17]
	global_load_dwordx4 v[158:161], v[212:213], off offset:3072
	global_load_dwordx4 v[154:157], v[214:215], off offset:3072
	ds_read_b128 v[166:169], v210 offset:224
	ds_read_b128 v[162:165], v210 offset:33504
	s_add_i32 s14, s14, 8
	v_add_u32_e32 v210, 0x100, v210
	s_cmp_lt_u32 s14, 16
	v_lshl_add_u64 v[180:181], v[180:181], 0, s[6:7]
	s_cbranch_scc1 .LBB3_21
	s_waitcnt vmcnt(15) lgkmcnt(3)
	v_mfma_f32_32x32x16_f16 v[50:65], v[118:121], v[174:177], v[50:65]
	s_waitcnt lgkmcnt(2)
	v_mfma_f32_32x32x16_f16 v[34:49], v[118:121], v[170:173], v[34:49]
	v_lshlrev_b32_e32 v118, 15, v209
	v_mov_b32_e32 v119, 0
	v_lshl_add_u64 v[120:121], s[0:1], 0, v[118:119]
	v_lshlrev_b32_e32 v118, 1, v178
	s_waitcnt vmcnt(14)
	v_mfma_f32_32x32x16_f16 v[18:33], v[98:101], v[174:177], v[18:33]
	v_lshl_add_u64 v[174:175], v[120:121], 0, v[118:119]
	ds_read_b128 v[118:121], v210
	ds_read_b128 v[212:215], v210 offset:33280
	v_mfma_f32_32x32x16_f16 v[2:17], v[98:101], v[170:173], v[2:17]
	s_waitcnt vmcnt(13) lgkmcnt(3)
	v_mfma_f32_32x32x16_f16 v[50:65], v[114:117], v[166:169], v[50:65]
	s_waitcnt lgkmcnt(2)
	v_mfma_f32_32x32x16_f16 v[34:49], v[114:117], v[162:165], v[34:49]
	ds_read_b128 v[98:101], v210 offset:32
	ds_read_b128 v[114:117], v210 offset:33312
	s_waitcnt vmcnt(12)
	v_mfma_f32_32x32x16_f16 v[18:33], v[102:105], v[166:169], v[18:33]
	v_mfma_f32_32x32x16_f16 v[2:17], v[102:105], v[162:165], v[2:17]
	s_waitcnt vmcnt(11) lgkmcnt(3)
	v_mfma_f32_32x32x16_f16 v[50:65], v[122:125], v[118:121], v[50:65]
	s_waitcnt lgkmcnt(2)
	v_mfma_f32_32x32x16_f16 v[34:49], v[122:125], v[212:215], v[34:49]
	s_waitcnt vmcnt(10)
	v_mfma_f32_32x32x16_f16 v[18:33], v[106:109], v[118:121], v[18:33]
	ds_read_b128 v[102:105], v210 offset:64
	ds_read_b128 v[118:121], v210 offset:33344
	v_mfma_f32_32x32x16_f16 v[2:17], v[106:109], v[212:215], v[2:17]
	s_waitcnt vmcnt(9) lgkmcnt(3)
	v_mfma_f32_32x32x16_f16 v[50:65], v[126:129], v[98:101], v[50:65]
	s_waitcnt lgkmcnt(2)
	v_mfma_f32_32x32x16_f16 v[34:49], v[126:129], v[114:117], v[34:49]
	s_waitcnt vmcnt(8)
	v_mfma_f32_32x32x16_f16 v[18:33], v[110:113], v[98:101], v[18:33]
	ds_read_b128 v[98:101], v210 offset:96
	ds_read_b128 v[106:109], v210 offset:33376
	v_mfma_f32_32x32x16_f16 v[2:17], v[110:113], v[114:117], v[2:17]
	s_waitcnt vmcnt(7) lgkmcnt(3)
	v_mfma_f32_32x32x16_f16 v[50:65], v[146:149], v[102:105], v[50:65]
	s_waitcnt lgkmcnt(2)
	v_mfma_f32_32x32x16_f16 v[34:49], v[146:149], v[118:121], v[34:49]
	s_waitcnt vmcnt(6)
	v_mfma_f32_32x32x16_f16 v[18:33], v[134:137], v[102:105], v[18:33]
	ds_read_b128 v[102:105], v210 offset:128
	ds_read_b128 v[110:113], v210 offset:33408
	v_mfma_f32_32x32x16_f16 v[2:17], v[134:137], v[118:121], v[2:17]
	s_waitcnt vmcnt(5) lgkmcnt(3)
	v_mfma_f32_32x32x16_f16 v[50:65], v[142:145], v[98:101], v[50:65]
	s_waitcnt lgkmcnt(2)
	v_mfma_f32_32x32x16_f16 v[34:49], v[142:145], v[106:109], v[34:49]
	s_waitcnt vmcnt(4)
	v_mfma_f32_32x32x16_f16 v[18:33], v[130:133], v[98:101], v[18:33]
	ds_read_b128 v[98:101], v210 offset:160
	ds_read_b128 v[114:117], v210 offset:33440
	v_mfma_f32_32x32x16_f16 v[2:17], v[130:133], v[106:109], v[2:17]
	s_waitcnt vmcnt(3) lgkmcnt(3)
	v_mfma_f32_32x32x16_f16 v[50:65], v[150:153], v[102:105], v[50:65]
	s_waitcnt lgkmcnt(2)
	v_mfma_f32_32x32x16_f16 v[34:49], v[150:153], v[110:113], v[34:49]
	s_waitcnt vmcnt(2)
	v_mfma_f32_32x32x16_f16 v[18:33], v[138:141], v[102:105], v[18:33]
	v_mfma_f32_32x32x16_f16 v[2:17], v[138:141], v[110:113], v[2:17]
	s_waitcnt vmcnt(1) lgkmcnt(1)
	v_mfma_f32_32x32x16_f16 v[50:65], v[158:161], v[98:101], v[50:65]
	s_waitcnt lgkmcnt(0)
	v_mfma_f32_32x32x16_f16 v[34:49], v[158:161], v[114:117], v[34:49]
	s_waitcnt vmcnt(0)
	v_mfma_f32_32x32x16_f16 v[18:33], v[154:157], v[98:101], v[18:33]
	v_mfma_f32_32x32x16_f16 v[2:17], v[154:157], v[114:117], v[2:17]
	v_readfirstlane_b32 s0, v209
	s_lshl_b32 s0, s0, 13
	s_cmp_lg_u32 0, -1
	s_cselect_b32 s1, 0, 0
	s_add_i32 s3, s1, s0
	s_mov_b64 s[0:1], 0x2000
	s_add_i32 s6, s3, 0x13400
	v_lshl_add_u64 v[98:99], v[174:175], 0, s[0:1]
	s_mov_b32 s7, m0
	s_mov_b32 m0, s6
	s_nop 0
	global_load_lds_dwordx4 v[98:99], off
	s_mov_b32 m0, s7
	s_mov_b64 s[6:7], 0x2400
	v_lshl_add_u64 v[98:99], v[174:175], 0, s[6:7]
	s_add_i32 s6, s3, 0x13800
	s_mov_b32 s7, m0
	s_mov_b32 m0, s6
	s_nop 0
	global_load_lds_dwordx4 v[98:99], off
	s_mov_b32 m0, s7
	s_mov_b64 s[6:7], 0x2800
	v_lshl_add_u64 v[98:99], v[174:175], 0, s[6:7]
	s_add_i32 s6, s3, 0x13c00
	s_mov_b32 s7, m0
	s_mov_b32 m0, s6
	s_nop 0
	global_load_lds_dwordx4 v[98:99], off
	s_mov_b32 m0, s7
	s_mov_b64 s[6:7], 0x2c00
	v_lshl_add_u64 v[98:99], v[174:175], 0, s[6:7]
	s_add_i32 s6, s3, 0x14000
	s_mov_b32 s7, m0
	s_mov_b32 m0, s6
	s_nop 0
	global_load_lds_dwordx4 v[98:99], off
	s_mov_b32 m0, s7
	s_mov_b64 s[6:7], 0x3000
	v_lshl_add_u64 v[98:99], v[174:175], 0, s[6:7]
	s_add_i32 s6, s3, 0x14400
	s_mov_b32 s7, m0
	s_mov_b32 m0, s6
	s_nop 0
	global_load_lds_dwordx4 v[98:99], off
	s_mov_b32 m0, s7
	s_mov_b64 s[6:7], 0x3400
	v_lshl_add_u64 v[98:99], v[174:175], 0, s[6:7]
	s_add_i32 s6, s3, 0x14800
	s_mov_b32 s7, m0
	s_mov_b32 m0, s6
	s_nop 0
	global_load_lds_dwordx4 v[98:99], off
	s_mov_b32 m0, s7
	s_mov_b64 s[6:7], 0x3800
	v_lshl_add_u64 v[98:99], v[174:175], 0, s[6:7]
	s_add_i32 s6, s3, 0x14c00
	s_mov_b32 s7, m0
	s_mov_b32 m0, s6
	s_nop 0
	global_load_lds_dwordx4 v[98:99], off
	s_mov_b32 m0, s7
	s_mov_b64 s[6:7], 0x3c00
	v_lshl_add_u64 v[98:99], v[174:175], 0, s[6:7]
	s_add_i32 s3, s3, 0x15000
	s_mov_b32 s6, m0
	s_mov_b32 m0, s3
	s_nop 0
	global_load_lds_dwordx4 v[98:99], off
	s_mov_b32 m0, s6
	global_load_dwordx4 v[126:129], v[174:175], off
	s_mov_b32 s3, 0
	global_load_dwordx4 v[122:125], v[174:175], off offset:1024
	global_load_dwordx4 v[118:121], v[174:175], off offset:2048
	global_load_dwordx4 v[114:117], v[174:175], off offset:3072
	s_movk_i32 s9, 0x1000
	v_add_co_u32_e32 v98, vcc, s9, v174
	s_nop 1
	v_addc_co_u32_e32 v99, vcc, 0, v175, vcc
	global_load_dwordx4 v[110:113], v[98:99], off
	global_load_dwordx4 v[106:109], v[98:99], off offset:1024
	global_load_dwordx4 v[102:105], v[98:99], off offset:2048
	s_nop 0
	global_load_dwordx4 v[98:101], v[98:99], off offset:3072
	v_and_b32_e32 v151, 0x1c0, v0
	v_lshlrev_b32_e32 v130, 2, v151
	s_add_i32 s6, 0, 0x11800
	v_lshlrev_b32_e32 v150, 4, v208
	v_add3_u32 v156, s6, v130, v150
	ds_read_b128 v[130:133], v156
	ds_read_b128 v[152:155], v156 offset:32
	ds_read_b128 v[210:213], v156 offset:64
	ds_read_b128 v[214:217], v156 offset:96
	ds_read_b128 v[218:221], v156 offset:160
	ds_read_b128 v[222:225], v156 offset:128
	ds_read_b128 v[226:229], v156 offset:192
	s_waitcnt lgkmcnt(6)
	v_pk_add_f32 v[148:149], v[130:131], v[50:51]
	s_nop 0
	v_add_f32_e32 v51, 0, v148
	v_mul_f32_e32 v50, v149, v149
	v_add_f32_e32 v134, v51, v149
	v_pk_add_f32 v[146:147], v[132:133], v[52:53]
	v_pk_fma_f32 v[50:51], v[148:149], v[148:149], v[50:51] op_sel_hi:[1,1,0]
	v_add_f32_e32 v52, v134, v146
	v_pk_add_f32 v[144:145], v[130:131], v[34:35]
	v_pk_fma_f32 v[50:51], v[146:147], v[146:147], v[50:51]
	v_add_f32_e32 v53, v52, v147
	v_mul_f32_e32 v52, v147, v147
	v_add_f32_e32 v34, 0, v144
	v_pk_add_f32 v[50:51], v[52:53], v[50:51] op_sel_hi:[0,1]
	v_add_f32_e32 v52, v34, v145
	v_mul_f32_e32 v34, v145, v145
	v_pk_add_f32 v[142:143], v[132:133], v[36:37]
	v_pk_fma_f32 v[34:35], v[144:145], v[144:145], v[34:35] op_sel_hi:[1,1,0]
	v_add_f32_e32 v36, v52, v142
	s_waitcnt lgkmcnt(5)
	v_pk_add_f32 v[140:141], v[152:153], v[54:55]
	v_pk_fma_f32 v[34:35], v[142:143], v[142:143], v[34:35]
	v_add_f32_e32 v52, v36, v143
	v_mul_f32_e32 v36, v143, v143
	v_add_f32_e32 v53, v53, v140
	v_pk_add_f32 v[34:35], v[36:37], v[34:35] op_sel_hi:[0,1]
	v_pk_fma_f32 v[36:37], v[140:141], v[140:141], v[50:51]
	v_add_f32_e32 v51, v53, v141
	v_mul_f32_e32 v50, v141, v141
	v_pk_add_f32 v[138:139], v[154:155], v[56:57]
	v_pk_add_f32 v[36:37], v[50:51], v[36:37] op_sel_hi:[0,1]
	v_add_f32_e32 v50, v51, v138
	v_pk_fma_f32 v[36:37], v[138:139], v[138:139], v[36:37]
	v_add_f32_e32 v54, v50, v139
	v_mul_f32_e32 v50, v139, v139
	v_pk_add_f32 v[136:137], v[152:153], v[38:39]
	v_pk_add_f32 v[50:51], v[50:51], v[36:37] op_sel_hi:[0,1]
	v_add_f32_e32 v36, v52, v136
	v_pk_fma_f32 v[34:35], v[136:137], v[136:137], v[34:35]
	v_add_f32_e32 v37, v36, v137
	v_mul_f32_e32 v36, v137, v137
	v_pk_add_f32 v[34:35], v[36:37], v[34:35] op_sel_hi:[0,1]
	v_pk_add_f32 v[132:133], v[154:155], v[40:41]
	s_nop 0
	v_add_f32_e32 v40, v37, v132
	v_pk_fma_f32 v[38:39], v[132:133], v[132:133], v[34:35]
	v_add_f32_e32 v55, v40, v133
	v_mul_f32_e32 v40, v133, v133
	v_pk_add_f32 v[52:53], v[40:41], v[38:39] op_sel_hi:[0,1]
	s_waitcnt lgkmcnt(4)
	v_pk_add_f32 v[134:135], v[210:211], v[58:59]
	v_pk_add_f32 v[130:131], v[212:213], v[60:61]
	v_add_f32_e32 v54, v54, v134
	v_pk_add_f32 v[60:61], v[210:211], v[42:43]
	v_pk_fma_f32 v[50:51], v[134:135], v[134:135], v[50:51]
	v_add_f32_e32 v56, v54, v135
	v_mul_f32_e32 v54, v135, v135
	v_add_f32_e32 v42, v55, v60
	v_pk_add_f32 v[50:51], v[54:55], v[50:51] op_sel_hi:[0,1]
	v_add_f32_e32 v54, v56, v130
	v_pk_fma_f32 v[34:35], v[60:61], v[60:61], v[52:53]
	v_add_f32_e32 v43, v42, v61
	v_mul_f32_e32 v42, v61, v61
	v_pk_add_f32 v[58:59], v[212:213], v[44:45]
	v_pk_fma_f32 v[50:51], v[130:131], v[130:131], v[50:51]
	v_add_f32_e32 v152, v54, v131
	v_mul_f32_e32 v54, v131, v131
	v_pk_add_f32 v[34:35], v[42:43], v[34:35] op_sel_hi:[0,1]
	v_add_f32_e32 v36, v43, v58
	s_waitcnt lgkmcnt(3)
	v_pk_add_f32 v[56:57], v[214:215], v[62:63]
	v_pk_add_f32 v[50:51], v[54:55], v[50:51] op_sel_hi:[0,1]
	v_pk_fma_f32 v[34:35], v[58:59], v[58:59], v[34:35]
	v_add_f32_e32 v44, v36, v59
	v_mul_f32_e32 v36, v59, v59
	v_add_f32_e32 v42, v152, v56
	v_pk_add_f32 v[34:35], v[36:37], v[34:35] op_sel_hi:[0,1]
	v_pk_fma_f32 v[36:37], v[56:57], v[56:57], v[50:51]
	v_add_f32_e32 v43, v42, v57
	v_mul_f32_e32 v42, v57, v57
	v_pk_add_f32 v[54:55], v[216:217], v[64:65]
	v_pk_add_f32 v[36:37], v[42:43], v[36:37] op_sel_hi:[0,1]
	v_add_f32_e32 v42, v43, v54
	v_pk_fma_f32 v[36:37], v[54:55], v[54:55], v[36:37]
	v_add_f32_e32 v45, v42, v55
	v_mul_f32_e32 v42, v55, v55
	v_pk_add_f32 v[52:53], v[214:215], v[46:47]
	v_pk_add_f32 v[42:43], v[42:43], v[36:37] op_sel_hi:[0,1]
	v_add_f32_e32 v36, v44, v52
	v_pk_fma_f32 v[34:35], v[52:53], v[52:53], v[34:35]
	v_add_f32_e32 v37, v36, v53
	v_mul_f32_e32 v36, v53, v53
	v_pk_add_f32 v[34:35], v[36:37], v[34:35] op_sel_hi:[0,1]
	v_pk_add_f32 v[50:51], v[216:217], v[48:49]
	v_add_f32_e32 v40, v37, v50
	v_pk_fma_f32 v[38:39], v[50:51], v[50:51], v[34:35]
	v_add_f32_e32 v41, v40, v51
	v_mul_f32_e32 v40, v51, v51
	v_pk_add_f32 v[38:39], v[40:41], v[38:39] op_sel_hi:[0,1]
	s_waitcnt lgkmcnt(1)
	v_pk_add_f32 v[48:49], v[222:223], v[18:19]
	s_nop 0
	v_add_f32_e32 v40, v45, v48
	v_pk_fma_f32 v[18:19], v[48:49], v[48:49], v[42:43]
	v_add_f32_e32 v42, v40, v49
	v_pk_add_f32 v[46:47], v[224:225], v[20:21]
	v_pk_add_f32 v[44:45], v[222:223], v[2:3]
	v_add_f32_e32 v20, v42, v46
	v_mul_f32_e32 v40, v49, v49
	v_add_f32_e32 v21, v20, v47
	v_add_f32_e32 v20, v41, v44
	v_pk_add_f32 v[18:19], v[40:41], v[18:19] op_sel_hi:[0,1]
	v_pk_fma_f32 v[2:3], v[44:45], v[44:45], v[38:39]
	v_add_f32_e32 v34, v20, v45
	v_mul_f32_e32 v20, v45, v45
	v_pk_add_f32 v[42:43], v[224:225], v[4:5]
	v_pk_add_f32 v[40:41], v[218:219], v[22:23]
	v_pk_fma_f32 v[18:19], v[46:47], v[46:47], v[18:19]
	v_pk_add_f32 v[2:3], v[20:21], v[2:3] op_sel_hi:[0,1]
	v_add_f32_e32 v4, v34, v42
	v_add_f32_e32 v21, v21, v40
	v_mul_f32_e32 v20, v47, v47
	v_add_f32_e32 v34, v4, v43
	v_mov_b32_e32 v4, v40
	v_mov_b32_e32 v5, v47
	v_pk_add_f32 v[18:19], v[20:21], v[18:19] op_sel_hi:[0,1]
	v_pk_fma_f32 v[4:5], v[4:5], v[4:5], v[18:19]
	v_add_f32_e32 v18, v21, v41
	v_pk_add_f32 v[38:39], v[220:221], v[24:25]
	v_mul_f32_e32 v20, v41, v41
	v_add_f32_e32 v21, v18, v38
	v_pk_fma_f32 v[2:3], v[42:43], v[42:43], v[2:3]
	v_mov_b32_e32 v18, v38
	v_mov_b32_e32 v19, v41
	v_pk_add_f32 v[4:5], v[20:21], v[4:5] op_sel_hi:[0,1]
	v_pk_add_f32 v[36:37], v[218:219], v[6:7]
	v_mul_f32_e32 v6, v43, v43
	v_pk_fma_f32 v[18:19], v[18:19], v[18:19], v[4:5]
	v_add_f32_e32 v20, v34, v36
	v_mov_b32_e32 v4, v36
	v_mov_b32_e32 v5, v43
	v_pk_add_f32 v[2:3], v[6:7], v[2:3] op_sel_hi:[0,1]
	v_pk_fma_f32 v[6:7], v[4:5], v[4:5], v[2:3]
	v_add_f32_e32 v2, v20, v37
	v_pk_add_f32 v[34:35], v[220:221], v[8:9]
	v_add_f32_e32 v21, v21, v39
	v_add_f32_e32 v22, v2, v34
	ds_read_b128 v[62:65], v156 offset:224
	v_mul_f32_e32 v20, v37, v37
	v_mov_b32_e32 v8, v34
	v_mov_b32_e32 v9, v37
	s_waitcnt lgkmcnt(1)
	v_pk_add_f32 v[26:27], v[226:227], v[26:27]
	v_pk_add_f32 v[6:7], v[20:21], v[6:7] op_sel_hi:[0,1]
	v_add_f32_e32 v21, v21, v26
	v_mul_f32_e32 v20, v39, v39
	v_pk_fma_f32 v[6:7], v[8:9], v[8:9], v[6:7]
	v_mov_b32_e32 v8, v26
	v_mov_b32_e32 v9, v39
	v_pk_add_f32 v[18:19], v[20:21], v[18:19] op_sel_hi:[0,1]
	v_pk_fma_f32 v[8:9], v[8:9], v[8:9], v[18:19]
	v_add_f32_e32 v18, v21, v27
	v_pk_add_f32 v[24:25], v[228:229], v[28:29]
	v_mul_f32_e32 v20, v27, v27
	v_add_f32_e32 v21, v18, v24
	v_add_f32_e32 v152, v22, v35
	v_mov_b32_e32 v18, v24
	v_mov_b32_e32 v19, v27
	v_pk_add_f32 v[8:9], v[20:21], v[8:9] op_sel_hi:[0,1]
	v_add_f32_e32 v28, v21, v25
	v_pk_add_f32 v[20:21], v[226:227], v[10:11]
	v_pk_fma_f32 v[22:23], v[18:19], v[18:19], v[8:9]
	v_add_f32_e32 v9, v152, v20
	v_mul_f32_e32 v8, v35, v35
	v_mov_b32_e32 v2, v20
	v_mov_b32_e32 v3, v35
	v_pk_add_f32 v[6:7], v[8:9], v[6:7] op_sel_hi:[0,1]
	v_pk_fma_f32 v[2:3], v[2:3], v[2:3], v[6:7]
	v_add_f32_e32 v6, v9, v21
	v_pk_add_f32 v[18:19], v[228:229], v[12:13]
	v_mov_b32_e32 v5, v21
	v_add_f32_e32 v7, v6, v18
	v_mul_f32_e32 v6, v21, v21
	v_mov_b32_e32 v4, v18
	v_pk_add_f32 v[2:3], v[6:7], v[2:3] op_sel_hi:[0,1]
	s_waitcnt lgkmcnt(0)
	v_pk_add_f32 v[8:9], v[62:63], v[30:31]
	v_mul_f32_e32 v6, v25, v25
	v_pk_fma_f32 v[2:3], v[4:5], v[4:5], v[2:3]
	v_add_f32_e32 v29, v7, v19
	v_mov_b32_e32 v4, v8
	v_mov_b32_e32 v5, v25
	v_pk_add_f32 v[6:7], v[6:7], v[22:23] op_sel_hi:[0,1]
	v_pk_fma_f32 v[4:5], v[4:5], v[4:5], v[6:7]
	v_pk_add_f32 v[6:7], v[64:65], v[32:33]
	v_mul_f32_e32 v22, v9, v9
	v_add_f32_e32 v10, v28, v8
	v_mov_b32_e32 v12, v6
	v_mov_b32_e32 v13, v9
	v_pk_add_f32 v[4:5], v[22:23], v[4:5] op_sel_hi:[0,1]
	v_add_f32_e32 v10, v10, v9
	v_pk_fma_f32 v[4:5], v[12:13], v[12:13], v[4:5]
	v_pk_mul_f32 v[12:13], v[6:7], v[6:7]
	v_add_f32_e32 v10, v10, v6
	v_mov_b32_e32 v11, v13
	v_pk_mov_b32 v[4:5], v[6:7], v[4:5] op_sel:[1,0]
	v_mov_b32_e32 v13, v19
	v_pk_add_f32 v[10:11], v[10:11], v[4:5]
	v_pk_add_f32 v[4:5], v[62:63], v[14:15]
	v_mul_f32_e32 v14, v19, v19
	v_add_f32_e32 v15, v29, v4
	v_mov_b32_e32 v12, v4
	v_pk_add_f32 v[2:3], v[14:15], v[2:3] op_sel_hi:[0,1]
	v_pk_fma_f32 v[12:13], v[12:13], v[12:13], v[2:3]
	v_pk_add_f32 v[2:3], v[64:65], v[16:17]
	v_mul_f32_e32 v22, v5, v5
	v_mov_b32_e32 v16, v2
	v_mov_b32_e32 v17, v5
	v_pk_add_f32 v[12:13], v[22:23], v[12:13] op_sel_hi:[0,1]
	v_add_f32_e32 v14, v15, v5
	v_pk_fma_f32 v[12:13], v[16:17], v[16:17], v[12:13]
	v_pk_mul_f32 v[16:17], v[2:3], v[2:3]
	v_add_f32_e32 v14, v14, v2
	v_mov_b32_e32 v15, v17
	v_pk_mov_b32 v[12:13], v[2:3], v[12:13] op_sel:[1,0]
	s_nop 0
	v_pk_add_f32 v[12:13], v[14:15], v[12:13]
	v_mbcnt_lo_u32_b32 v14, -1, 0
	v_mbcnt_hi_u32_b32 v14, -1, v14
	v_and_b32_e32 v16, 64, v14
	v_xor_b32_e32 v15, 32, v14
	v_add_u32_e32 v16, 64, v16
	v_cmp_lt_i32_e32 vcc, v15, v16
	s_nop 1
	v_cndmask_b32_e32 v14, v14, v15, vcc
	v_lshlrev_b32_e32 v17, 2, v14
	ds_bpermute_b32 v14, v17, v10
	ds_bpermute_b32 v15, v17, v11
	ds_bpermute_b32 v16, v17, v12
	ds_bpermute_b32 v17, v17, v13
	v_cmp_gt_u32_e32 vcc, 32, v206
	s_and_saveexec_b64 s[6:7], vcc
	s_cbranch_execz .LBB3_24
	s_waitcnt lgkmcnt(2)
	v_pk_add_f32 v[10:11], v[10:11], v[14:15]
	v_and_b32_e32 v14, 0x1df, v0
	s_add_i32 s8, 0, 0x10400
	v_lshl_add_u32 v14, v14, 3, s8
	ds_write_b64 v14, v[10:11]
	v_mov_b32_e32 v10, 0x100
	v_lshl_or_b32 v10, v0, 3, v10
	s_waitcnt lgkmcnt(1)
	v_pk_add_f32 v[12:13], v[12:13], v[16:17]
	v_add_u32_e32 v10, s8, v10
	ds_write_b64 v10, v[12:13]
